# peel+nt plus static s_setprio 1 for waves 4-7 (younger half) during the mixer phases (retA/glaA/pool, retB/glaB)
# speedup vs baseline: 1.0034x; 1.0034x over previous
.LBB0_518:
	v_readlane_b32 s0, v254, 63
	v_readlane_b32 s1, v255, 0
	s_andn2_b64 vcc, exec, s[0:1]
	s_cbranch_vccnz .LBB0_668
	s_mov_b32 s0, -1
	v_readlane_b32 s2, v253, 35
	v_mbcnt_lo_u32_b32 v0, s0, 0
	v_mbcnt_hi_u32_b32 v0, s0, v0
	v_readlane_b32 s0, v253, 49
	v_readlane_b32 s3, v253, 36
	s_load_dwordx2 s[2:3], s[2:3], 0x80
	v_add_u32_e32 v48, s0, v0
	v_readlane_b32 s0, v255, 11
	v_readlane_b32 s1, v255, 12
	s_mov_b32 s4, s1
	v_readlane_b32 s0, v253, 47
	v_readlane_b32 s1, v253, 48
	s_load_dword s5, s[0:1], 0x0
	v_readlane_b32 s0, v253, 0
	v_readfirstlane_b32 s1, v48
	s_waitcnt lgkmcnt(0)
	v_readlane_b32 s100, v253, 41
	s_cmp_lt_u32 s100, 4
	s_cbranch_scc1 .Lprio_skip_mixa
	s_setprio 1
.Lprio_skip_mixa:
	s_cmpk_gt_i32 s0, 0x2ff
	s_cbranch_scc1 .LBB0_524
	s_add_u32 s8, s2, 0x45000000
	s_addc_u32 s13, s3, 0
	s_ashr_i32 s15, s0, 31
	s_lshr_b32 s15, s15, 27
	s_add_i32 s15, s0, s15
	s_ashr_i32 s16, s15, 5
	s_and_b32 s15, s15, 0x1ffffe0
	s_sub_i32 s15, s0, s15
	s_lshl_b32 s18, s15, 7
	s_ashr_i32 s17, s16, 31
	s_ashr_i32 s19, s18, 31
	s_ashr_i32 s1, s1, 6
	s_lshl_b64 s[16:17], s[16:17], 19
	s_lshl_b64 s[18:19], s[18:19], 7
	s_add_u32 s18, s18, s16
	s_addc_u32 s19, s19, s17
	s_add_u32 s15, s2, 0x26800000
	s_addc_u32 s16, s3, 0
	s_lshl_b64 s[18:19], s[18:19], 1
	s_add_u32 s20, s15, s18
	s_addc_u32 s21, s16, s19
	s_add_u32 s2, s2, 0x28000000
	v_lshlrev_b32_e32 v212, 3, v48
	s_addc_u32 s3, s3, 0
	s_waitcnt vmcnt(0)
	v_lshlrev_b64 v[16:17], 1, v[212:213]
	v_add_u32_e32 v2, 0x1000, v212
	v_mov_b32_e32 v3, v213
	v_add_u32_e32 v8, 0x2000, v212
	v_mov_b32_e32 v9, v213
	v_add_u32_e32 v212, 0x3000, v212
	s_add_u32 s18, s2, s18
	v_lshlrev_b64 v[18:19], 1, v[2:3]
	v_lshlrev_b64 v[24:25], 1, v[8:9]
	v_lshlrev_b64 v[26:27], 1, v[212:213]
	s_addc_u32 s19, s3, s19
	v_lshl_add_u64 v[0:1], s[20:21], 0, v[16:17]
	v_lshl_add_u64 v[4:5], s[20:21], 0, v[18:19]
	v_lshl_add_u64 v[8:9], s[20:21], 0, v[24:25]
	v_lshl_add_u64 v[12:13], s[20:21], 0, v[26:27]
	v_lshl_add_u64 v[16:17], s[18:19], 0, v[16:17]
	v_lshl_add_u64 v[20:21], s[18:19], 0, v[18:19]
	v_lshl_add_u64 v[24:25], s[18:19], 0, v[24:25]
	v_lshl_add_u64 v[28:29], s[18:19], 0, v[26:27]
	global_load_dwordx4 v[0:3], v[0:1], off
	s_nop 0
	global_load_dwordx4 v[4:7], v[4:5], off
	s_nop 0
	global_load_dwordx4 v[8:11], v[8:9], off
	s_nop 0
	global_load_dwordx4 v[12:15], v[12:13], off
	s_nop 0
	global_load_dwordx4 v[16:19], v[16:17], off
	s_nop 0
	global_load_dwordx4 v[20:23], v[20:21], off
	s_nop 0
	global_load_dwordx4 v[24:27], v[24:25], off
	s_nop 0
	global_load_dwordx4 v[28:31], v[28:29], off
	s_lshl_b32 s17, s1, 5
	s_lshl_b32 s18, s1, 11
	s_add_i32 s1, s0, s5
	s_lshl_b32 s19, s1, 7
	s_lshl_b32 s20, s5, 7
	s_branch .LBB0_522

.LBB0_618:
	s_setprio 0
	v_readlane_b32 s0, v253, 42
	v_readlane_b32 s1, v253, 43
	s_andn2_b64 vcc, exec, s[0:1]
	s_cbranch_vccnz .LBB0_668
	s_mov_b32 s0, -1
	s_waitcnt vmcnt(0)
	s_nop 0
	v_mbcnt_lo_u32_b32 v0, s0, 0
	v_mbcnt_hi_u32_b32 v0, s0, v0
	v_readlane_b32 s0, v253, 50
	s_barrier
	s_nop 0
	v_cmp_eq_u32_e32 vcc, s0, v0
	s_and_saveexec_b64 s[0:1], vcc
	s_cbranch_execz .LBB0_667
	v_readlane_b32 s2, v253, 44
	s_waitcnt vmcnt(0) expcnt(0) lgkmcnt(0)
	s_nop 0
	v_mov_b32_e32 v0, s2
	ds_read_b32 v2, v0
	ds_read_b32 v0, v0 offset:4
	s_waitcnt lgkmcnt(1)
	v_cmp_ne_u32_e32 vcc, 0, v2
	s_cbranch_vccnz .LBB0_635
	v_readlane_b32 s4, v253, 47
	v_readlane_b32 s5, v253, 48
	s_load_dwordx2 s[2:3], s[4:5], 0x0
	s_nop 0
	s_load_dword s4, s[4:5], 0x8
	s_mov_b32 s13, 1
	s_waitcnt lgkmcnt(0)
	s_mul_i32 s8, s3, s2
	s_mul_i32 s8, s8, s4
	s_branch .LBB0_623

.LBB0_726:
	v_readlane_b32 s0, v255, 3
	v_readlane_b32 s1, v255, 4
	s_andn2_b64 vcc, exec, s[0:1]
	s_cbranch_vccnz .LBB0_1035
	s_mov_b32 s0, -1
	s_nop 0
	v_mbcnt_lo_u32_b32 v0, s0, 0
	v_mbcnt_hi_u32_b32 v0, s0, v0
	v_readlane_b32 s0, v253, 49
	s_nop 1
	v_add_u32_e32 v215, s0, v0
	v_readlane_b32 s0, v255, 11
	v_readlane_b32 s1, v255, 12
	s_mov_b32 s15, s1
	v_readlane_b32 s0, v253, 47
	v_readlane_b32 s1, v253, 48
	s_load_dword s16, s[0:1], 0x0
	v_readlane_b32 s0, v253, 0
	s_mov_b32 s96, s0
	v_readlane_b32 s0, v253, 35
	v_readlane_b32 s1, v253, 36
	v_readfirstlane_b32 s4, v215
	s_waitcnt lgkmcnt(0)
	s_load_dwordx2 s[0:1], s[0:1], 0x80
	v_readlane_b32 s100, v253, 41
	s_cmp_lt_u32 s100, 4
	s_cbranch_scc1 .Lprio_skip_mixb
	s_setprio 1
.Lprio_skip_mixb:
	s_cmpk_gt_i32 s96, 0x2ff
	s_waitcnt lgkmcnt(0)
	s_cbranch_scc1 .LBB0_902
	s_add_u32 s18, s0, 0x25000000
	s_addc_u32 s28, s1, 0
	s_add_u32 s17, s0, 0x31000000
	s_addc_u32 s30, s1, 0
	s_add_u32 s8, s0, 0x48000000
	s_addc_u32 s13, s1, 0
	s_ashr_i32 s97, s96, 31
	s_lshr_b32 s2, s97, 27
	s_add_i32 s3, s96, s2
	s_ashr_i32 s2, s3, 5
	s_and_b32 s3, s3, 0x1ffffe0
	s_sub_i32 s19, s96, s3
	s_lshl_b32 s20, s19, 7
	s_ashr_i32 s3, s2, 31
	s_ashr_i32 s21, s20, 31
	s_add_i32 s56, s15, 0x12000
	s_add_i32 s57, s15, 0x1b800
	s_ashr_i32 s5, s4, 6
	s_lshl_b64 s[2:3], s[2:3], 19
	s_lshl_b64 s[20:21], s[20:21], 7
	s_add_u32 s2, s20, s2
	s_addc_u32 s3, s21, s3
	s_lshl_b64 s[2:3], s[2:3], 1
	s_add_u32 s20, s18, s2
	s_addc_u32 s21, s28, s3
	v_lshlrev_b32_e32 v212, 3, v215
	v_lshlrev_b64 v[48:49], 1, v[212:213]
	v_add_u32_e32 v2, 0x1000, v212
	v_mov_b32_e32 v3, v213
	s_waitcnt vmcnt(0)
	v_add_u32_e32 v8, 0x2000, v212
	v_mov_b32_e32 v9, v213
	v_add_u32_e32 v212, 0x3000, v212
	s_add_u32 s58, s0, 0x26800000
	v_lshlrev_b64 v[50:51], 1, v[2:3]
	v_lshlrev_b64 v[56:57], 1, v[8:9]
	v_lshlrev_b64 v[58:59], 1, v[212:213]
	s_addc_u32 s59, s1, 0
	v_lshl_add_u64 v[0:1], s[20:21], 0, v[48:49]
	v_lshl_add_u64 v[4:5], s[20:21], 0, v[50:51]
	v_lshl_add_u64 v[8:9], s[20:21], 0, v[56:57]
	v_lshl_add_u64 v[10:11], s[20:21], 0, v[58:59]
	s_add_u32 s20, s58, s2
	s_addc_u32 s21, s59, s3
	s_add_u32 s60, s0, 0x28000000
	s_addc_u32 s61, s1, 0
	global_load_dwordx4 v[0:3], v[0:1], off
	s_nop 0
	global_load_dwordx4 v[4:7], v[4:5], off
	s_nop 0
	global_load_dwordx4 v[16:19], v[8:9], off
	global_load_dwordx4 v[20:23], v[10:11], off
	v_lshl_add_u64 v[8:9], s[20:21], 0, v[48:49]
	s_add_u32 s2, s60, s2
	v_lshl_add_u64 v[10:11], s[20:21], 0, v[50:51]
	global_load_dwordx4 v[32:35], v[8:9], off
	global_load_dwordx4 v[36:39], v[10:11], off
	v_lshl_add_u64 v[8:9], s[20:21], 0, v[56:57]
	s_addc_u32 s3, s61, s3
	v_lshl_add_u64 v[10:11], s[20:21], 0, v[58:59]
	global_load_dwordx4 v[40:43], v[8:9], off
	global_load_dwordx4 v[44:47], v[10:11], off
	v_lshl_add_u64 v[8:9], s[2:3], 0, v[48:49]
	s_waitcnt vmcnt(19)
	v_lshl_add_u64 v[12:13], s[2:3], 0, v[50:51]
	s_waitcnt vmcnt(17)
	v_lshl_add_u64 v[24:25], s[2:3], 0, v[56:57]
	s_waitcnt vmcnt(16)
	v_lshl_add_u64 v[28:29], s[2:3], 0, v[58:59]
	s_lshl_b64 s[2:3], s[96:97], 15
	s_add_u32 s2, s8, s2
	s_addc_u32 s3, s13, s3
	v_lshl_add_u64 v[48:49], s[2:3], 0, v[48:49]
	v_lshl_add_u64 v[52:53], s[2:3], 0, v[50:51]
	v_lshl_add_u64 v[56:57], s[2:3], 0, v[56:57]
	v_lshl_add_u64 v[60:61], s[2:3], 0, v[58:59]
	global_load_dwordx4 v[8:11], v[8:9], off
	s_nop 0
	global_load_dwordx4 v[12:15], v[12:13], off
	s_nop 0
	global_load_dwordx4 v[24:27], v[24:25], off
	s_nop 0
	global_load_dwordx4 v[28:31], v[28:29], off
	s_nop 0
	global_load_dwordx4 v[48:51], v[48:49], off
	s_nop 0
	global_load_dwordx4 v[52:55], v[52:53], off
	s_nop 0
	global_load_dwordx4 v[56:59], v[56:57], off
	s_nop 0
	global_load_dwordx4 v[60:63], v[60:61], off
	s_lshl_b32 s68, s5, 4
	s_cmp_lt_u32 s4, 64
	s_cselect_b64 s[20:21], -1, 0
	s_cmp_lt_i32 s5, 2
	s_cselect_b64 s[34:35], -1, 0
	s_cmp_lt_i32 s5, 1
	s_cselect_b64 s[62:63], -1, 0
	s_cmp_lt_i32 s5, 3
	s_cselect_b64 s[80:81], -1, 0
	s_cmp_lt_i32 s5, 4
	s_cselect_b64 s[86:87], -1, 0
	s_cmp_lt_i32 s5, 5
	s_cselect_b64 s[88:89], -1, 0
	s_cmp_lt_i32 s5, 6
	s_cselect_b64 s[90:91], -1, 0
	s_cmp_lt_i32 s5, 7
	s_cselect_b64 s[24:25], -1, 0
	s_cmp_lt_i32 s5, 8
	s_cselect_b64 s[94:95], -1, 0
	s_add_u32 s69, s0, 0x29800000
	s_addc_u32 s70, s1, 0
	s_lshl_b32 s0, s5, 5
	s_add_i32 s71, s15, s0
	s_cmp_eq_u32 s5, 1
	s_cselect_b64 s[64:65], -1, 0
	s_cmp_eq_u32 s5, 2
	s_cselect_b64 s[2:3], -1, 0
	s_cmp_eq_u32 s5, 3
	s_cselect_b64 s[22:23], -1, 0
	s_cmp_eq_u32 s5, 4
	s_cselect_b64 s[92:93], -1, 0
	s_cmp_eq_u32 s5, 5
	s_cselect_b64 s[66:67], -1, 0
	s_cmp_eq_u32 s5, 6
	s_cselect_b64 s[72:73], -1, 0
	s_cmp_eq_u32 s5, 7
	s_cselect_b64 s[74:75], -1, 0
	s_ashr_i32 s0, s4, 7
	s_cmp_gt_i32 s0, -1
	s_cselect_b64 s[76:77], -1, 0
	s_cmp_gt_i32 s0, 0
	s_cselect_b64 s[78:79], -1, 0
	s_cmp_gt_i32 s0, 1
	s_cselect_b64 s[82:83], -1, 0
	s_cmp_gt_i32 s0, 2
	s_cselect_b64 s[84:85], -1, 0
	s_lshl_b32 s97, s96, 7
	s_lshl_b32 s19, s16, 7
	s_branch .LBB0_730

	.amdhsa_kernel _Z3fwd4Args
		.amdhsa_group_segment_fixed_size 0
		.amdhsa_private_segment_fixed_size 0
		.amdhsa_kernarg_size 416
		.amdhsa_user_sgpr_count 2
		.amdhsa_user_sgpr_dispatch_ptr 0
		.amdhsa_user_sgpr_queue_ptr 0
		.amdhsa_user_sgpr_kernarg_segment_ptr 1
		.amdhsa_user_sgpr_dispatch_id 0
		.amdhsa_user_sgpr_kernarg_preload_length 0
		.amdhsa_user_sgpr_kernarg_preload_offset 0
		.amdhsa_user_sgpr_private_segment_size 0
		.amdhsa_uses_dynamic_stack 0
		.amdhsa_enable_private_segment 0
		.amdhsa_system_sgpr_workgroup_id_x 1
		.amdhsa_system_sgpr_workgroup_id_y 0
		.amdhsa_system_sgpr_workgroup_id_z 0
		.amdhsa_system_sgpr_workgroup_info 0
		.amdhsa_system_vgpr_workitem_id 0
		.amdhsa_next_free_vgpr 256
		.amdhsa_next_free_sgpr 102
		.amdhsa_accum_offset 256
		.amdhsa_reserve_vcc 1
		.amdhsa_float_round_mode_32 0
		.amdhsa_float_round_mode_16_64 0
		.amdhsa_float_denorm_mode_32 3
		.amdhsa_float_denorm_mode_16_64 3
		.amdhsa_dx10_clamp 1
		.amdhsa_ieee_mode 1
		.amdhsa_fp16_overflow 0
		.amdhsa_tg_split 0
		.amdhsa_exception_fp_ieee_invalid_op 0
		.amdhsa_exception_fp_denorm_src 0
		.amdhsa_exception_fp_ieee_div_zero 0
		.amdhsa_exception_fp_ieee_overflow 0
		.amdhsa_exception_fp_ieee_underflow 0
		.amdhsa_exception_fp_ieee_inexact 0
		.amdhsa_exception_int_div_zero 0
	.end_amdhsa_kernel

amdhsa.kernels:
  - .agpr_count:     0
    .args:
      - .offset:         0
        .size:           160
        .value_kind:     by_value
      - .offset:         160
        .size:           4
        .value_kind:     hidden_block_count_x
      - .offset:         164
        .size:           4
        .value_kind:     hidden_block_count_y
      - .offset:         168
        .size:           4
        .value_kind:     hidden_block_count_z
      - .offset:         172
        .size:           2
        .value_kind:     hidden_group_size_x
      - .offset:         174
        .size:           2
        .value_kind:     hidden_group_size_y
      - .offset:         176
        .size:           2
        .value_kind:     hidden_group_size_z
      - .offset:         178
        .size:           2
        .value_kind:     hidden_remainder_x
      - .offset:         180
        .size:           2
        .value_kind:     hidden_remainder_y
      - .offset:         182
        .size:           2
        .value_kind:     hidden_remainder_z
      - .offset:         200
        .size:           8
        .value_kind:     hidden_global_offset_x
      - .offset:         208
        .size:           8
        .value_kind:     hidden_global_offset_y
      - .offset:         216
        .size:           8
        .value_kind:     hidden_global_offset_z
      - .offset:         224
        .size:           2
        .value_kind:     hidden_grid_dims
      - .offset:         280
        .size:           4
        .value_kind:     hidden_dynamic_lds_size
    .group_segment_fixed_size: 0
    .kernarg_segment_align: 8
    .kernarg_segment_size: 416
    .language:       OpenCL C
    .language_version:
      - 2
      - 0
    .max_flat_workgroup_size: 512
    .name:           _Z3fwd4Args
    .private_segment_fixed_size: 0
    .sgpr_count:     108
    .sgpr_spill_count: 167
    .symbol:         _Z3fwd4Args.kd
    .uniform_work_group_size: 1
    .uses_dynamic_stack: false
    .vgpr_count:     256
    .vgpr_spill_count: 0
    .wavefront_size: 64
